# baseline (speedup 1.0000x reference)
.Lou_loop:
	s_waitcnt lgkmcnt(0)
	v_mfma_f32_16x16x32_bf16 v[64:67], v[176:179], v[160:163], v[64:67]
	ds_read_b128 v[200:203], v11 offset:0
	v_mfma_f32_16x16x32_bf16 v[68:71], v[176:179], v[164:167], v[68:71]
	s_add_u32 m0, s20, 0x5000
	v_mfma_f32_16x16x32_bf16 v[72:75], v[176:179], v[168:171], v[72:75]
	ds_read_b128 v[204:207], v11 offset:2048
	v_mfma_f32_16x16x32_bf16 v[76:79], v[176:179], v[172:175], v[76:79]
	global_load_lds_dwordx4 v3, s[18:19]
	v_mfma_f32_16x16x32_bf16 v[80:83], v[180:183], v[160:163], v[80:83]
	ds_read_b128 v[208:211], v11 offset:4096
	v_mfma_f32_16x16x32_bf16 v[84:87], v[180:183], v[164:167], v[84:87]
	s_add_u32 m0, s20, 0x6000
	v_mfma_f32_16x16x32_bf16 v[88:91], v[180:183], v[168:171], v[88:91]
	ds_read_b128 v[212:215], v11 offset:6144
	v_mfma_f32_16x16x32_bf16 v[92:95], v[180:183], v[172:175], v[92:95]
	global_load_lds_dwordx4 v4, s[18:19]
	v_mfma_f32_16x16x32_bf16 v[96:99], v[184:187], v[160:163], v[96:99]
	ds_read_b128 v[216:219], v13 offset:0
	v_mfma_f32_16x16x32_bf16 v[100:103], v[184:187], v[164:167], v[100:103]
	s_add_u32 m0, s20, 0x7000
	v_mfma_f32_16x16x32_bf16 v[104:107], v[184:187], v[168:171], v[104:107]
	ds_read_b128 v[220:223], v13 offset:2048
	v_mfma_f32_16x16x32_bf16 v[108:111], v[184:187], v[172:175], v[108:111]
	global_load_lds_dwordx4 v5, s[18:19]
	v_mfma_f32_16x16x32_bf16 v[112:115], v[188:191], v[160:163], v[112:115]
	ds_read_b128 v[224:227], v13 offset:4096
	v_mfma_f32_16x16x32_bf16 v[116:119], v[188:191], v[164:167], v[116:119]
	s_add_u32 m0, s20, 0x8000
	v_mfma_f32_16x16x32_bf16 v[120:123], v[188:191], v[168:171], v[120:123]
	ds_read_b128 v[228:231], v13 offset:6144
	v_mfma_f32_16x16x32_bf16 v[124:127], v[188:191], v[172:175], v[124:127]
	global_load_lds_dwordx4 v6, s[18:19]
	v_mfma_f32_16x16x32_bf16 v[128:131], v[192:195], v[160:163], v[128:131]
	ds_read_b128 v[232:235], v13 offset:8192
	v_mfma_f32_16x16x32_bf16 v[132:135], v[192:195], v[164:167], v[132:135]
	s_add_u32 m0, s20, 0x9000
	v_mfma_f32_16x16x32_bf16 v[136:139], v[192:195], v[168:171], v[136:139]
	ds_read_b128 v[236:239], v13 offset:10240
	v_mfma_f32_16x16x32_bf16 v[140:143], v[192:195], v[172:175], v[140:143]
	global_load_lds_dwordx4 v7, s[18:19]
	v_mfma_f32_16x16x32_bf16 v[144:147], v[196:199], v[160:163], v[144:147]
	s_add_u32 s16, s16, 0x80
	s_addc_u32 s17, s17, 0
	s_add_u32 s18, s18, 0x80
	s_addc_u32 s19, s19, 0
	v_mfma_f32_16x16x32_bf16 v[148:151], v[196:199], v[164:167], v[148:151]
	s_add_u32 s20, s20, 0xa000
	s_sub_u32 s22, s20, 0x28000
	s_cmp_ge_u32 s20, 0x28000
	s_cselect_b32 s20, s22, s20
	v_mfma_f32_16x16x32_bf16 v[152:155], v[196:199], v[168:171], v[152:155]
	v_add_u32_e32 v10, s21, v8
	v_add_u32_e32 v12, s21, v9
	v_xor_b32_e32 v11, 64, v10
	v_xor_b32_e32 v13, 64, v12
	v_mfma_f32_16x16x32_bf16 v[156:159], v[196:199], v[172:175], v[156:159]
	s_add_u32 s21, s21, 0xa000
	s_sub_u32 s23, s21, 0x28000
	s_cmp_ge_u32 s21, 0x28000
	s_cselect_b32 s21, s23, s21
	s_waitcnt lgkmcnt(0)
	v_mfma_f32_16x16x32_bf16 v[64:67], v[216:219], v[200:203], v[64:67]
	v_mfma_f32_16x16x32_bf16 v[68:71], v[216:219], v[204:207], v[68:71]
	v_mfma_f32_16x16x32_bf16 v[72:75], v[216:219], v[208:211], v[72:75]
	v_mfma_f32_16x16x32_bf16 v[76:79], v[216:219], v[212:215], v[76:79]
	s_waitcnt vmcnt(20)
	s_barrier
	v_mfma_f32_16x16x32_bf16 v[80:83], v[220:223], v[200:203], v[80:83]
	ds_read_b128 v[160:163], v10 offset:0
	v_mfma_f32_16x16x32_bf16 v[84:87], v[220:223], v[204:207], v[84:87]
	s_add_u32 m0, s20, 0x0
	v_mfma_f32_16x16x32_bf16 v[88:91], v[220:223], v[208:211], v[88:91]
	ds_read_b128 v[164:167], v10 offset:2048
	v_mfma_f32_16x16x32_bf16 v[92:95], v[220:223], v[212:215], v[92:95]
	global_load_lds_dwordx4 v2, s[16:17]
	v_mfma_f32_16x16x32_bf16 v[96:99], v[224:227], v[200:203], v[96:99]
	ds_read_b128 v[168:171], v10 offset:4096
	v_mfma_f32_16x16x32_bf16 v[100:103], v[224:227], v[204:207], v[100:103]
	s_add_u32 m0, s20, 0x1000
	v_mfma_f32_16x16x32_bf16 v[104:107], v[224:227], v[208:211], v[104:107]
	ds_read_b128 v[172:175], v10 offset:6144
	v_mfma_f32_16x16x32_bf16 v[108:111], v[224:227], v[212:215], v[108:111]
	global_load_lds_dwordx4 v3, s[16:17]
	v_mfma_f32_16x16x32_bf16 v[112:115], v[228:231], v[200:203], v[112:115]
	ds_read_b128 v[176:179], v12 offset:0
	v_mfma_f32_16x16x32_bf16 v[116:119], v[228:231], v[204:207], v[116:119]
	s_add_u32 m0, s20, 0x2000
	v_mfma_f32_16x16x32_bf16 v[120:123], v[228:231], v[208:211], v[120:123]
	ds_read_b128 v[180:183], v12 offset:2048
	v_mfma_f32_16x16x32_bf16 v[124:127], v[228:231], v[212:215], v[124:127]
	global_load_lds_dwordx4 v4, s[16:17]
	v_mfma_f32_16x16x32_bf16 v[128:131], v[232:235], v[200:203], v[128:131]
	ds_read_b128 v[184:187], v12 offset:4096
	v_mfma_f32_16x16x32_bf16 v[132:135], v[232:235], v[204:207], v[132:135]
	s_add_u32 m0, s20, 0x3000
	v_mfma_f32_16x16x32_bf16 v[136:139], v[232:235], v[208:211], v[136:139]
	ds_read_b128 v[188:191], v12 offset:6144
	v_mfma_f32_16x16x32_bf16 v[140:143], v[232:235], v[212:215], v[140:143]
	global_load_lds_dwordx4 v5, s[16:17]
	v_mfma_f32_16x16x32_bf16 v[144:147], v[236:239], v[200:203], v[144:147]
	ds_read_b128 v[192:195], v12 offset:8192
	v_mfma_f32_16x16x32_bf16 v[148:151], v[236:239], v[204:207], v[148:151]
	s_add_u32 m0, s20, 0x4000
	v_mfma_f32_16x16x32_bf16 v[152:155], v[236:239], v[208:211], v[152:155]
	ds_read_b128 v[196:199], v12 offset:10240
	v_mfma_f32_16x16x32_bf16 v[156:159], v[236:239], v[212:215], v[156:159]
	global_load_lds_dwordx4 v2, s[18:19]
	s_add_u32 s15, s15, 1
	s_cmp_lt_u32 s15, 8
	s_cbranch_scc1 .Lou_loop
	s_waitcnt lgkmcnt(0)
	v_mfma_f32_16x16x32_bf16 v[64:67], v[176:179], v[160:163], v[64:67]
	ds_read_b128 v[200:203], v11 offset:0
	v_mfma_f32_16x16x32_bf16 v[68:71], v[176:179], v[164:167], v[68:71]
	s_add_u32 m0, s20, 0x5000
	v_mfma_f32_16x16x32_bf16 v[72:75], v[176:179], v[168:171], v[72:75]
	ds_read_b128 v[204:207], v11 offset:2048
	v_mfma_f32_16x16x32_bf16 v[76:79], v[176:179], v[172:175], v[76:79]
	global_load_lds_dwordx4 v3, s[18:19]
	v_mfma_f32_16x16x32_bf16 v[80:83], v[180:183], v[160:163], v[80:83]
	ds_read_b128 v[208:211], v11 offset:4096
	v_mfma_f32_16x16x32_bf16 v[84:87], v[180:183], v[164:167], v[84:87]
	s_add_u32 m0, s20, 0x6000
	v_mfma_f32_16x16x32_bf16 v[88:91], v[180:183], v[168:171], v[88:91]
	ds_read_b128 v[212:215], v11 offset:6144
	v_mfma_f32_16x16x32_bf16 v[92:95], v[180:183], v[172:175], v[92:95]
	global_load_lds_dwordx4 v4, s[18:19]
	v_mfma_f32_16x16x32_bf16 v[96:99], v[184:187], v[160:163], v[96:99]
	ds_read_b128 v[216:219], v13 offset:0
	v_mfma_f32_16x16x32_bf16 v[100:103], v[184:187], v[164:167], v[100:103]
	s_add_u32 m0, s20, 0x7000
	v_mfma_f32_16x16x32_bf16 v[104:107], v[184:187], v[168:171], v[104:107]
	ds_read_b128 v[220:223], v13 offset:2048
	v_mfma_f32_16x16x32_bf16 v[108:111], v[184:187], v[172:175], v[108:111]
	global_load_lds_dwordx4 v5, s[18:19]
	v_mfma_f32_16x16x32_bf16 v[112:115], v[188:191], v[160:163], v[112:115]
	ds_read_b128 v[224:227], v13 offset:4096
	v_mfma_f32_16x16x32_bf16 v[116:119], v[188:191], v[164:167], v[116:119]
	s_add_u32 m0, s20, 0x8000
	v_mfma_f32_16x16x32_bf16 v[120:123], v[188:191], v[168:171], v[120:123]
	ds_read_b128 v[228:231], v13 offset:6144
	v_mfma_f32_16x16x32_bf16 v[124:127], v[188:191], v[172:175], v[124:127]
	global_load_lds_dwordx4 v6, s[18:19]
	v_mfma_f32_16x16x32_bf16 v[128:131], v[192:195], v[160:163], v[128:131]
	ds_read_b128 v[232:235], v13 offset:8192
	v_mfma_f32_16x16x32_bf16 v[132:135], v[192:195], v[164:167], v[132:135]
	s_add_u32 m0, s20, 0x9000
	v_mfma_f32_16x16x32_bf16 v[136:139], v[192:195], v[168:171], v[136:139]
	ds_read_b128 v[236:239], v13 offset:10240
	v_mfma_f32_16x16x32_bf16 v[140:143], v[192:195], v[172:175], v[140:143]
	global_load_lds_dwordx4 v7, s[18:19]
	v_mfma_f32_16x16x32_bf16 v[144:147], v[196:199], v[160:163], v[144:147]
	s_add_u32 s16, s16, 0x80
	s_addc_u32 s17, s17, 0
	s_add_u32 s18, s18, 0x80
	s_addc_u32 s19, s19, 0
	v_mfma_f32_16x16x32_bf16 v[148:151], v[196:199], v[164:167], v[148:151]
	s_add_u32 s20, s20, 0xa000
	s_sub_u32 s22, s20, 0x28000
	s_cmp_ge_u32 s20, 0x28000
	s_cselect_b32 s20, s22, s20
	v_mfma_f32_16x16x32_bf16 v[152:155], v[196:199], v[168:171], v[152:155]
	v_add_u32_e32 v10, s21, v8
	v_add_u32_e32 v12, s21, v9
	v_xor_b32_e32 v11, 64, v10
	v_xor_b32_e32 v13, 64, v12
	v_mfma_f32_16x16x32_bf16 v[156:159], v[196:199], v[172:175], v[156:159]
	s_add_u32 s21, s21, 0xa000
	s_sub_u32 s23, s21, 0x28000
	s_cmp_ge_u32 s21, 0x28000
	s_cselect_b32 s21, s23, s21
	s_waitcnt lgkmcnt(0)
	v_mfma_f32_16x16x32_bf16 v[64:67], v[216:219], v[200:203], v[64:67]
	v_mfma_f32_16x16x32_bf16 v[68:71], v[216:219], v[204:207], v[68:71]
	v_mfma_f32_16x16x32_bf16 v[72:75], v[216:219], v[208:211], v[72:75]
	v_mfma_f32_16x16x32_bf16 v[76:79], v[216:219], v[212:215], v[76:79]
	s_waitcnt vmcnt(20)
	s_barrier
	v_mfma_f32_16x16x32_bf16 v[80:83], v[220:223], v[200:203], v[80:83]
	ds_read_b128 v[160:163], v10 offset:0
	v_mfma_f32_16x16x32_bf16 v[84:87], v[220:223], v[204:207], v[84:87]
	ds_read_b128 v[164:167], v10 offset:2048
	v_mfma_f32_16x16x32_bf16 v[88:91], v[220:223], v[208:211], v[88:91]
	ds_read_b128 v[168:171], v10 offset:4096
	v_mfma_f32_16x16x32_bf16 v[92:95], v[220:223], v[212:215], v[92:95]
	ds_read_b128 v[172:175], v10 offset:6144
	v_mfma_f32_16x16x32_bf16 v[96:99], v[224:227], v[200:203], v[96:99]
	ds_read_b128 v[176:179], v12 offset:0
	v_mfma_f32_16x16x32_bf16 v[100:103], v[224:227], v[204:207], v[100:103]
	ds_read_b128 v[180:183], v12 offset:2048
	v_mfma_f32_16x16x32_bf16 v[104:107], v[224:227], v[208:211], v[104:107]
	ds_read_b128 v[184:187], v12 offset:4096
	v_mfma_f32_16x16x32_bf16 v[108:111], v[224:227], v[212:215], v[108:111]
	ds_read_b128 v[188:191], v12 offset:6144
	v_mfma_f32_16x16x32_bf16 v[112:115], v[228:231], v[200:203], v[112:115]
	ds_read_b128 v[192:195], v12 offset:8192
	v_mfma_f32_16x16x32_bf16 v[116:119], v[228:231], v[204:207], v[116:119]
	ds_read_b128 v[196:199], v12 offset:10240
	v_mfma_f32_16x16x32_bf16 v[120:123], v[228:231], v[208:211], v[120:123]
	v_mfma_f32_16x16x32_bf16 v[124:127], v[228:231], v[212:215], v[124:127]
	v_mfma_f32_16x16x32_bf16 v[128:131], v[232:235], v[200:203], v[128:131]
	v_mfma_f32_16x16x32_bf16 v[132:135], v[232:235], v[204:207], v[132:135]
	v_mfma_f32_16x16x32_bf16 v[136:139], v[232:235], v[208:211], v[136:139]
	v_mfma_f32_16x16x32_bf16 v[140:143], v[232:235], v[212:215], v[140:143]
	v_mfma_f32_16x16x32_bf16 v[144:147], v[236:239], v[200:203], v[144:147]
	v_mfma_f32_16x16x32_bf16 v[148:151], v[236:239], v[204:207], v[148:151]
	v_mfma_f32_16x16x32_bf16 v[152:155], v[236:239], v[208:211], v[152:155]
	v_mfma_f32_16x16x32_bf16 v[156:159], v[236:239], v[212:215], v[156:159]
	s_waitcnt lgkmcnt(0)
	v_mfma_f32_16x16x32_bf16 v[64:67], v[176:179], v[160:163], v[64:67]
	ds_read_b128 v[200:203], v11 offset:0
	v_mfma_f32_16x16x32_bf16 v[68:71], v[176:179], v[164:167], v[68:71]
	ds_read_b128 v[204:207], v11 offset:2048
	v_mfma_f32_16x16x32_bf16 v[72:75], v[176:179], v[168:171], v[72:75]
	ds_read_b128 v[208:211], v11 offset:4096
	v_mfma_f32_16x16x32_bf16 v[76:79], v[176:179], v[172:175], v[76:79]
	ds_read_b128 v[212:215], v11 offset:6144
	v_mfma_f32_16x16x32_bf16 v[80:83], v[180:183], v[160:163], v[80:83]
	ds_read_b128 v[216:219], v13 offset:0
	v_mfma_f32_16x16x32_bf16 v[84:87], v[180:183], v[164:167], v[84:87]
	ds_read_b128 v[220:223], v13 offset:2048
	v_mfma_f32_16x16x32_bf16 v[88:91], v[180:183], v[168:171], v[88:91]
	ds_read_b128 v[224:227], v13 offset:4096
	v_mfma_f32_16x16x32_bf16 v[92:95], v[180:183], v[172:175], v[92:95]
	ds_read_b128 v[228:231], v13 offset:6144
	v_mfma_f32_16x16x32_bf16 v[96:99], v[184:187], v[160:163], v[96:99]
	ds_read_b128 v[232:235], v13 offset:8192
	v_mfma_f32_16x16x32_bf16 v[100:103], v[184:187], v[164:167], v[100:103]
	ds_read_b128 v[236:239], v13 offset:10240
	v_mfma_f32_16x16x32_bf16 v[104:107], v[184:187], v[168:171], v[104:107]
	v_mfma_f32_16x16x32_bf16 v[108:111], v[184:187], v[172:175], v[108:111]
	v_mfma_f32_16x16x32_bf16 v[112:115], v[188:191], v[160:163], v[112:115]
	v_mfma_f32_16x16x32_bf16 v[116:119], v[188:191], v[164:167], v[116:119]
	v_mfma_f32_16x16x32_bf16 v[120:123], v[188:191], v[168:171], v[120:123]
	v_mfma_f32_16x16x32_bf16 v[124:127], v[188:191], v[172:175], v[124:127]
	v_mfma_f32_16x16x32_bf16 v[128:131], v[192:195], v[160:163], v[128:131]
	v_mfma_f32_16x16x32_bf16 v[132:135], v[192:195], v[164:167], v[132:135]
	v_mfma_f32_16x16x32_bf16 v[136:139], v[192:195], v[168:171], v[136:139]
	v_mfma_f32_16x16x32_bf16 v[140:143], v[192:195], v[172:175], v[140:143]
	v_mfma_f32_16x16x32_bf16 v[144:147], v[196:199], v[160:163], v[144:147]
	v_add_u32_e32 v10, s21, v8
	v_add_u32_e32 v12, s21, v9
	v_xor_b32_e32 v11, 64, v10
	v_xor_b32_e32 v13, 64, v12
	v_mfma_f32_16x16x32_bf16 v[148:151], v[196:199], v[164:167], v[148:151]
	s_add_u32 s21, s21, 0xa000
	s_sub_u32 s23, s21, 0x28000
	s_cmp_ge_u32 s21, 0x28000
	s_cselect_b32 s21, s23, s21
	v_mfma_f32_16x16x32_bf16 v[152:155], v[196:199], v[168:171], v[152:155]
	v_mfma_f32_16x16x32_bf16 v[156:159], v[196:199], v[172:175], v[156:159]
	s_waitcnt lgkmcnt(0)
	v_mfma_f32_16x16x32_bf16 v[64:67], v[216:219], v[200:203], v[64:67]
	v_mfma_f32_16x16x32_bf16 v[68:71], v[216:219], v[204:207], v[68:71]
	v_mfma_f32_16x16x32_bf16 v[72:75], v[216:219], v[208:211], v[72:75]
	v_mfma_f32_16x16x32_bf16 v[76:79], v[216:219], v[212:215], v[76:79]
	s_waitcnt vmcnt(10)
	s_barrier
	v_mfma_f32_16x16x32_bf16 v[80:83], v[220:223], v[200:203], v[80:83]
	ds_read_b128 v[160:163], v10 offset:0
	v_mfma_f32_16x16x32_bf16 v[84:87], v[220:223], v[204:207], v[84:87]
	ds_read_b128 v[164:167], v10 offset:2048
	v_mfma_f32_16x16x32_bf16 v[88:91], v[220:223], v[208:211], v[88:91]
	ds_read_b128 v[168:171], v10 offset:4096
	v_mfma_f32_16x16x32_bf16 v[92:95], v[220:223], v[212:215], v[92:95]
	ds_read_b128 v[172:175], v10 offset:6144
	v_mfma_f32_16x16x32_bf16 v[96:99], v[224:227], v[200:203], v[96:99]
	ds_read_b128 v[176:179], v12 offset:0
	v_mfma_f32_16x16x32_bf16 v[100:103], v[224:227], v[204:207], v[100:103]
	ds_read_b128 v[180:183], v12 offset:2048
	v_mfma_f32_16x16x32_bf16 v[104:107], v[224:227], v[208:211], v[104:107]
	ds_read_b128 v[184:187], v12 offset:4096
	v_mfma_f32_16x16x32_bf16 v[108:111], v[224:227], v[212:215], v[108:111]
	ds_read_b128 v[188:191], v12 offset:6144
	v_mfma_f32_16x16x32_bf16 v[112:115], v[228:231], v[200:203], v[112:115]
	ds_read_b128 v[192:195], v12 offset:8192
	v_mfma_f32_16x16x32_bf16 v[116:119], v[228:231], v[204:207], v[116:119]
	ds_read_b128 v[196:199], v12 offset:10240
	v_mfma_f32_16x16x32_bf16 v[120:123], v[228:231], v[208:211], v[120:123]
	v_mfma_f32_16x16x32_bf16 v[124:127], v[228:231], v[212:215], v[124:127]
	v_mfma_f32_16x16x32_bf16 v[128:131], v[232:235], v[200:203], v[128:131]
	v_mfma_f32_16x16x32_bf16 v[132:135], v[232:235], v[204:207], v[132:135]
	v_mfma_f32_16x16x32_bf16 v[136:139], v[232:235], v[208:211], v[136:139]
	v_mfma_f32_16x16x32_bf16 v[140:143], v[232:235], v[212:215], v[140:143]
	v_mfma_f32_16x16x32_bf16 v[144:147], v[236:239], v[200:203], v[144:147]
	v_mfma_f32_16x16x32_bf16 v[148:151], v[236:239], v[204:207], v[148:151]
	v_mfma_f32_16x16x32_bf16 v[152:155], v[236:239], v[208:211], v[152:155]
	v_mfma_f32_16x16x32_bf16 v[156:159], v[236:239], v[212:215], v[156:159]
	s_waitcnt lgkmcnt(0)
	v_mfma_f32_16x16x32_bf16 v[64:67], v[176:179], v[160:163], v[64:67]
	ds_read_b128 v[200:203], v11 offset:0
	v_mfma_f32_16x16x32_bf16 v[68:71], v[176:179], v[164:167], v[68:71]
	ds_read_b128 v[204:207], v11 offset:2048
	v_mfma_f32_16x16x32_bf16 v[72:75], v[176:179], v[168:171], v[72:75]
	ds_read_b128 v[208:211], v11 offset:4096
	v_mfma_f32_16x16x32_bf16 v[76:79], v[176:179], v[172:175], v[76:79]
	ds_read_b128 v[212:215], v11 offset:6144
	v_mfma_f32_16x16x32_bf16 v[80:83], v[180:183], v[160:163], v[80:83]
	ds_read_b128 v[216:219], v13 offset:0
	v_mfma_f32_16x16x32_bf16 v[84:87], v[180:183], v[164:167], v[84:87]
	ds_read_b128 v[220:223], v13 offset:2048
	v_mfma_f32_16x16x32_bf16 v[88:91], v[180:183], v[168:171], v[88:91]
	ds_read_b128 v[224:227], v13 offset:4096
	v_mfma_f32_16x16x32_bf16 v[92:95], v[180:183], v[172:175], v[92:95]
	ds_read_b128 v[228:231], v13 offset:6144
	v_mfma_f32_16x16x32_bf16 v[96:99], v[184:187], v[160:163], v[96:99]
	ds_read_b128 v[232:235], v13 offset:8192
	v_mfma_f32_16x16x32_bf16 v[100:103], v[184:187], v[164:167], v[100:103]
	ds_read_b128 v[236:239], v13 offset:10240
	v_mfma_f32_16x16x32_bf16 v[104:107], v[184:187], v[168:171], v[104:107]
	v_mfma_f32_16x16x32_bf16 v[108:111], v[184:187], v[172:175], v[108:111]
	v_mfma_f32_16x16x32_bf16 v[112:115], v[188:191], v[160:163], v[112:115]
	v_mfma_f32_16x16x32_bf16 v[116:119], v[188:191], v[164:167], v[116:119]
	v_mfma_f32_16x16x32_bf16 v[120:123], v[188:191], v[168:171], v[120:123]
	v_mfma_f32_16x16x32_bf16 v[124:127], v[188:191], v[172:175], v[124:127]
	v_mfma_f32_16x16x32_bf16 v[128:131], v[192:195], v[160:163], v[128:131]
	v_mfma_f32_16x16x32_bf16 v[132:135], v[192:195], v[164:167], v[132:135]
	v_mfma_f32_16x16x32_bf16 v[136:139], v[192:195], v[168:171], v[136:139]
	v_mfma_f32_16x16x32_bf16 v[140:143], v[192:195], v[172:175], v[140:143]
	v_mfma_f32_16x16x32_bf16 v[144:147], v[196:199], v[160:163], v[144:147]
	v_add_u32_e32 v10, s21, v8
	v_add_u32_e32 v12, s21, v9
	v_xor_b32_e32 v11, 64, v10
	v_xor_b32_e32 v13, 64, v12
	v_mfma_f32_16x16x32_bf16 v[148:151], v[196:199], v[164:167], v[148:151]
	s_add_u32 s21, s21, 0xa000
	s_sub_u32 s23, s21, 0x28000
	s_cmp_ge_u32 s21, 0x28000
	s_cselect_b32 s21, s23, s21
	v_mfma_f32_16x16x32_bf16 v[152:155], v[196:199], v[168:171], v[152:155]
	v_mfma_f32_16x16x32_bf16 v[156:159], v[196:199], v[172:175], v[156:159]
	s_waitcnt lgkmcnt(0)
	v_mfma_f32_16x16x32_bf16 v[64:67], v[216:219], v[200:203], v[64:67]
	v_mfma_f32_16x16x32_bf16 v[68:71], v[216:219], v[204:207], v[68:71]
	v_mfma_f32_16x16x32_bf16 v[72:75], v[216:219], v[208:211], v[72:75]
	v_mfma_f32_16x16x32_bf16 v[76:79], v[216:219], v[212:215], v[76:79]
	s_waitcnt vmcnt(0)
	s_barrier
	v_mfma_f32_16x16x32_bf16 v[80:83], v[220:223], v[200:203], v[80:83]
	ds_read_b128 v[160:163], v10 offset:0
	v_mfma_f32_16x16x32_bf16 v[84:87], v[220:223], v[204:207], v[84:87]
	global_load_dwordx4 v[16:19], v56, s[8:9] offset:0
	v_mfma_f32_16x16x32_bf16 v[88:91], v[220:223], v[208:211], v[88:91]
	ds_read_b128 v[164:167], v10 offset:2048
	v_mfma_f32_16x16x32_bf16 v[92:95], v[220:223], v[212:215], v[92:95]
	global_load_dwordx4 v[20:23], v57, s[8:9] offset:0
	v_mfma_f32_16x16x32_bf16 v[96:99], v[224:227], v[200:203], v[96:99]
	ds_read_b128 v[168:171], v10 offset:4096
	v_mfma_f32_16x16x32_bf16 v[100:103], v[224:227], v[204:207], v[100:103]
	global_load_dwordx4 v[24:27], v58, s[8:9] offset:0
	v_mfma_f32_16x16x32_bf16 v[104:107], v[224:227], v[208:211], v[104:107]
	ds_read_b128 v[172:175], v10 offset:6144
	v_mfma_f32_16x16x32_bf16 v[108:111], v[224:227], v[212:215], v[108:111]
	global_load_dwordx4 v[28:31], v59, s[8:9] offset:0
	v_mfma_f32_16x16x32_bf16 v[112:115], v[228:231], v[200:203], v[112:115]
	ds_read_b128 v[176:179], v12 offset:0
	v_mfma_f32_16x16x32_bf16 v[116:119], v[228:231], v[204:207], v[116:119]
	global_load_dwordx4 v[32:35], v56, s[8:9] offset:64
	v_mfma_f32_16x16x32_bf16 v[120:123], v[228:231], v[208:211], v[120:123]
	ds_read_b128 v[180:183], v12 offset:2048
	v_mfma_f32_16x16x32_bf16 v[124:127], v[228:231], v[212:215], v[124:127]
	global_load_dwordx4 v[36:39], v57, s[8:9] offset:64
	v_mfma_f32_16x16x32_bf16 v[128:131], v[232:235], v[200:203], v[128:131]
	ds_read_b128 v[184:187], v12 offset:4096
	v_mfma_f32_16x16x32_bf16 v[132:135], v[232:235], v[204:207], v[132:135]
	global_load_dwordx4 v[40:43], v58, s[8:9] offset:64
	v_mfma_f32_16x16x32_bf16 v[136:139], v[232:235], v[208:211], v[136:139]
	ds_read_b128 v[188:191], v12 offset:6144
	v_mfma_f32_16x16x32_bf16 v[140:143], v[232:235], v[212:215], v[140:143]
	global_load_dwordx4 v[44:47], v59, s[8:9] offset:64
	v_mfma_f32_16x16x32_bf16 v[144:147], v[236:239], v[200:203], v[144:147]
	ds_read_b128 v[192:195], v12 offset:8192
	v_mfma_f32_16x16x32_bf16 v[148:151], v[236:239], v[204:207], v[148:151]
	global_load_dwordx4 v[48:51], v56, s[8:9] offset:128
	v_mfma_f32_16x16x32_bf16 v[152:155], v[236:239], v[208:211], v[152:155]
	ds_read_b128 v[196:199], v12 offset:10240
	v_mfma_f32_16x16x32_bf16 v[156:159], v[236:239], v[212:215], v[156:159]
	global_load_dwordx4 v[52:55], v57, s[8:9] offset:128
	global_load_dwordx4 v[240:243], v58, s[8:9] offset:128
	global_load_dwordx4 v[244:247], v59, s[8:9] offset:128
	global_load_dwordx4 v[248:251], v56, s[8:9] offset:192
	global_load_dwordx4 v[252:255], v57, s[8:9] offset:192
	s_waitcnt lgkmcnt(0)
	v_mfma_f32_16x16x32_bf16 v[64:67], v[176:179], v[160:163], v[64:67]
	ds_read_b128 v[200:203], v11 offset:0
	v_mfma_f32_16x16x32_bf16 v[68:71], v[176:179], v[164:167], v[68:71]
	ds_read_b128 v[204:207], v11 offset:2048
	v_mfma_f32_16x16x32_bf16 v[72:75], v[176:179], v[168:171], v[72:75]
	ds_read_b128 v[208:211], v11 offset:4096
	v_mfma_f32_16x16x32_bf16 v[76:79], v[176:179], v[172:175], v[76:79]
	ds_read_b128 v[212:215], v11 offset:6144
	v_mfma_f32_16x16x32_bf16 v[80:83], v[180:183], v[160:163], v[80:83]
	ds_read_b128 v[216:219], v13 offset:0
	v_mfma_f32_16x16x32_bf16 v[84:87], v[180:183], v[164:167], v[84:87]
	ds_read_b128 v[220:223], v13 offset:2048
	v_mfma_f32_16x16x32_bf16 v[88:91], v[180:183], v[168:171], v[88:91]
	ds_read_b128 v[224:227], v13 offset:4096
	v_mfma_f32_16x16x32_bf16 v[92:95], v[180:183], v[172:175], v[92:95]
	ds_read_b128 v[228:231], v13 offset:6144
	v_mfma_f32_16x16x32_bf16 v[96:99], v[184:187], v[160:163], v[96:99]
	ds_read_b128 v[232:235], v13 offset:8192
	v_mfma_f32_16x16x32_bf16 v[100:103], v[184:187], v[164:167], v[100:103]
	ds_read_b128 v[236:239], v13 offset:10240
	v_mfma_f32_16x16x32_bf16 v[104:107], v[184:187], v[168:171], v[104:107]
	v_mfma_f32_16x16x32_bf16 v[108:111], v[184:187], v[172:175], v[108:111]
	v_mfma_f32_16x16x32_bf16 v[112:115], v[188:191], v[160:163], v[112:115]
	v_mfma_f32_16x16x32_bf16 v[116:119], v[188:191], v[164:167], v[116:119]
	v_mfma_f32_16x16x32_bf16 v[120:123], v[188:191], v[168:171], v[120:123]
	v_mfma_f32_16x16x32_bf16 v[124:127], v[188:191], v[172:175], v[124:127]
	v_mfma_f32_16x16x32_bf16 v[128:131], v[192:195], v[160:163], v[128:131]
	v_mfma_f32_16x16x32_bf16 v[132:135], v[192:195], v[164:167], v[132:135]
	v_mfma_f32_16x16x32_bf16 v[136:139], v[192:195], v[168:171], v[136:139]
	v_mfma_f32_16x16x32_bf16 v[140:143], v[192:195], v[172:175], v[140:143]
	v_mfma_f32_16x16x32_bf16 v[144:147], v[196:199], v[160:163], v[144:147]
	v_mfma_f32_16x16x32_bf16 v[148:151], v[196:199], v[164:167], v[148:151]
	v_mfma_f32_16x16x32_bf16 v[152:155], v[196:199], v[168:171], v[152:155]
	v_mfma_f32_16x16x32_bf16 v[156:159], v[196:199], v[172:175], v[156:159]
	s_waitcnt lgkmcnt(0)
	v_mfma_f32_16x16x32_bf16 v[64:67], v[216:219], v[200:203], v[64:67]
	v_mfma_f32_16x16x32_bf16 v[68:71], v[216:219], v[204:207], v[68:71]
	global_load_dwordx4 v[160:163], v58, s[8:9] offset:192
	v_mfma_f32_16x16x32_bf16 v[72:75], v[216:219], v[208:211], v[72:75]
	v_mfma_f32_16x16x32_bf16 v[76:79], v[216:219], v[212:215], v[76:79]
	global_load_dwordx4 v[164:167], v59, s[8:9] offset:192
	v_mfma_f32_16x16x32_bf16 v[80:83], v[220:223], v[200:203], v[80:83]
	v_mfma_f32_16x16x32_bf16 v[84:87], v[220:223], v[204:207], v[84:87]
	global_load_dwordx4 v[168:171], v56, s[8:9] offset:256
	v_mfma_f32_16x16x32_bf16 v[88:91], v[220:223], v[208:211], v[88:91]
	v_mfma_f32_16x16x32_bf16 v[92:95], v[220:223], v[212:215], v[92:95]
	global_load_dwordx4 v[172:175], v57, s[8:9] offset:256
	v_mfma_f32_16x16x32_bf16 v[96:99], v[224:227], v[200:203], v[96:99]
	v_mfma_f32_16x16x32_bf16 v[100:103], v[224:227], v[204:207], v[100:103]
	global_load_dwordx4 v[176:179], v58, s[8:9] offset:256
	v_mfma_f32_16x16x32_bf16 v[104:107], v[224:227], v[208:211], v[104:107]
	v_mfma_f32_16x16x32_bf16 v[108:111], v[224:227], v[212:215], v[108:111]
	global_load_dwordx4 v[180:183], v59, s[8:9] offset:256
	v_mfma_f32_16x16x32_bf16 v[112:115], v[228:231], v[200:203], v[112:115]
	v_mfma_f32_16x16x32_bf16 v[116:119], v[228:231], v[204:207], v[116:119]
	global_load_dwordx4 v[184:187], v56, s[8:9] offset:320
	v_mfma_f32_16x16x32_bf16 v[120:123], v[228:231], v[208:211], v[120:123]
	v_mfma_f32_16x16x32_bf16 v[124:127], v[228:231], v[212:215], v[124:127]
	global_load_dwordx4 v[188:191], v57, s[8:9] offset:320
	v_mfma_f32_16x16x32_bf16 v[128:131], v[232:235], v[200:203], v[128:131]
	v_mfma_f32_16x16x32_bf16 v[132:135], v[232:235], v[204:207], v[132:135]
	global_load_dwordx4 v[192:195], v58, s[8:9] offset:320
	v_mfma_f32_16x16x32_bf16 v[136:139], v[232:235], v[208:211], v[136:139]
	v_mfma_f32_16x16x32_bf16 v[140:143], v[232:235], v[212:215], v[140:143]
	global_load_dwordx4 v[196:199], v59, s[8:9] offset:320
	v_mfma_f32_16x16x32_bf16 v[144:147], v[236:239], v[200:203], v[144:147]
	v_mfma_f32_16x16x32_bf16 v[148:151], v[236:239], v[204:207], v[148:151]
	v_mfma_f32_16x16x32_bf16 v[152:155], v[236:239], v[208:211], v[152:155]
	v_mfma_f32_16x16x32_bf16 v[156:159], v[236:239], v[212:215], v[156:159]
	v_and_b32_e32 v12, 63, v0
	v_cmp_gt_u32_e32 vcc, 16, v12
	v_xor_b32_e32 v13, 16, v12
	v_lshlrev_b32_e32 v13, 2, v13
	v_xor_b32_e32 v12, 32, v12
	v_lshlrev_b32_e32 v12, 2, v12
	v_bfe_u32 v14, v0, 6, 1
	v_mul_u32_u24_e32 v14, 0x60, v14
	v_bfe_u32 v15, v0, 4, 2
	v_lshl_add_u32 v14, v15, 2, v14
	v_add_u32_e32 v14, s13, v14
	v_lshlrev_b32_e32 v14, 2, v14
	global_load_dwordx4 v[200:203], v14, s[24:25]
	global_load_dwordx4 v[204:207], v14, s[24:25] offset:64
	global_load_dwordx4 v[208:211], v14, s[24:25] offset:128
	global_load_dwordx4 v[212:215], v14, s[24:25] offset:192
	global_load_dwordx4 v[216:219], v14, s[24:25] offset:256
	global_load_dwordx4 v[220:223], v14, s[24:25] offset:320
	v_lshrrev_b32_e32 v60, 1, v56
	v_lshrrev_b32_e32 v61, 1, v57
	v_lshrrev_b32_e32 v62, 1, v58
	v_lshrrev_b32_e32 v63, 1, v59
	v_bfe_u32 v8, v0, 7, 1
	v_and_b32_e32 v9, 15, v0
	v_lshl_add_u32 v8, v8, 6, v9
	v_add_u32_e32 v8, s12, v8
	v_lshlrev_b32_e32 v8, 6, v8
	v_bfe_u32 v9, v0, 6, 1
	v_lshlrev_b32_e32 v9, 1, v9
	v_add_u32_e32 v9, s30, v9
	v_lshl_add_u32 v8, v9, 2, v8
	v_add_u32_e32 v9, 0x400, v8
	v_add_u32_e32 v10, 0x400, v9
	v_add_u32_e32 v11, 0x400, v10
	s_waitcnt vmcnt(0)
	v_pk_add_f32 v[64:65], v[64:65], v[16:17]
	v_pk_add_f32 v[66:67], v[66:67], v[18:19]
	global_store_dwordx4 v56, v[64:67], s[10:11]
	v_pk_mul_f32 v[224:225], v[200:201], v[64:65]
	v_pk_mul_f32 v[226:227], v[202:203], v[66:67]
	v_cvt_pk_bf16_f32 v228, v224, v225
	v_cvt_pk_bf16_f32 v229, v226, v227
	global_store_dwordx2 v60, v[228:229], s[28:29]
	v_pk_mul_f32 v[230:231], v[64:65], v[64:65]
	v_pk_mul_f32 v[232:233], v[66:67], v[66:67]
	v_add_f32_e32 v230, v230, v231
	v_add_f32_e32 v230, v232, v230
	v_add_f32_e32 v234, v233, v230
	v_pk_add_f32 v[80:81], v[80:81], v[32:33]
	v_pk_add_f32 v[82:83], v[82:83], v[34:35]
	global_store_dwordx4 v56, v[80:83], s[10:11] offset:64
	v_pk_mul_f32 v[224:225], v[204:205], v[80:81]
	v_pk_mul_f32 v[226:227], v[206:207], v[82:83]
	v_cvt_pk_bf16_f32 v228, v224, v225
	v_cvt_pk_bf16_f32 v229, v226, v227
	global_store_dwordx2 v60, v[228:229], s[28:29] offset:32
	v_pk_mul_f32 v[230:231], v[80:81], v[80:81]
	v_pk_mul_f32 v[232:233], v[82:83], v[82:83]
	v_add_f32_e32 v230, v230, v231
	v_add_f32_e32 v230, v232, v230
	v_add_f32_e32 v230, v233, v230
	v_add_f32_e32 v234, v234, v230
	v_pk_add_f32 v[96:97], v[96:97], v[48:49]
	v_pk_add_f32 v[98:99], v[98:99], v[50:51]
	global_store_dwordx4 v56, v[96:99], s[10:11] offset:128
	v_pk_mul_f32 v[224:225], v[208:209], v[96:97]
	v_pk_mul_f32 v[226:227], v[210:211], v[98:99]
	v_cvt_pk_bf16_f32 v228, v224, v225
	v_cvt_pk_bf16_f32 v229, v226, v227
	global_store_dwordx2 v60, v[228:229], s[28:29] offset:64
	v_pk_mul_f32 v[230:231], v[96:97], v[96:97]
	v_pk_mul_f32 v[232:233], v[98:99], v[98:99]
	v_add_f32_e32 v230, v230, v231
	v_add_f32_e32 v230, v232, v230
	v_add_f32_e32 v230, v233, v230
	v_add_f32_e32 v234, v234, v230
	v_pk_add_f32 v[112:113], v[112:113], v[248:249]
	v_pk_add_f32 v[114:115], v[114:115], v[250:251]
	global_store_dwordx4 v56, v[112:115], s[10:11] offset:192
	v_pk_mul_f32 v[224:225], v[212:213], v[112:113]
	v_pk_mul_f32 v[226:227], v[214:215], v[114:115]
	v_cvt_pk_bf16_f32 v228, v224, v225
	v_cvt_pk_bf16_f32 v229, v226, v227
	global_store_dwordx2 v60, v[228:229], s[28:29] offset:96
	v_pk_mul_f32 v[230:231], v[112:113], v[112:113]
	v_pk_mul_f32 v[232:233], v[114:115], v[114:115]
	v_add_f32_e32 v230, v230, v231
	v_add_f32_e32 v230, v232, v230
	v_add_f32_e32 v235, v233, v230
	v_pk_add_f32 v[128:129], v[128:129], v[168:169]
	v_pk_add_f32 v[130:131], v[130:131], v[170:171]
	global_store_dwordx4 v56, v[128:131], s[10:11] offset:256
	v_pk_mul_f32 v[224:225], v[216:217], v[128:129]
	v_pk_mul_f32 v[226:227], v[218:219], v[130:131]
	v_cvt_pk_bf16_f32 v228, v224, v225
	v_cvt_pk_bf16_f32 v229, v226, v227
	global_store_dwordx2 v60, v[228:229], s[28:29] offset:128
	v_pk_mul_f32 v[230:231], v[128:129], v[128:129]
	v_pk_mul_f32 v[232:233], v[130:131], v[130:131]
	v_add_f32_e32 v230, v230, v231
	v_add_f32_e32 v230, v232, v230
	v_add_f32_e32 v230, v233, v230
	v_add_f32_e32 v235, v235, v230
	v_pk_add_f32 v[144:145], v[144:145], v[184:185]
	v_pk_add_f32 v[146:147], v[146:147], v[186:187]
	global_store_dwordx4 v56, v[144:147], s[10:11] offset:320
	v_pk_mul_f32 v[224:225], v[220:221], v[144:145]
	v_pk_mul_f32 v[226:227], v[222:223], v[146:147]
	v_cvt_pk_bf16_f32 v228, v224, v225
	v_cvt_pk_bf16_f32 v229, v226, v227
	global_store_dwordx2 v60, v[228:229], s[28:29] offset:160
	v_pk_mul_f32 v[230:231], v[144:145], v[144:145]
	v_pk_mul_f32 v[232:233], v[146:147], v[146:147]
	v_add_f32_e32 v230, v230, v231
	v_add_f32_e32 v230, v232, v230
	v_add_f32_e32 v230, v233, v230
	v_add_f32_e32 v235, v235, v230
	v_pk_add_f32 v[68:69], v[68:69], v[20:21]
	v_pk_add_f32 v[70:71], v[70:71], v[22:23]
	global_store_dwordx4 v57, v[68:71], s[10:11]
	v_pk_mul_f32 v[224:225], v[200:201], v[68:69]
	v_pk_mul_f32 v[226:227], v[202:203], v[70:71]
	v_cvt_pk_bf16_f32 v228, v224, v225
	v_cvt_pk_bf16_f32 v229, v226, v227
	global_store_dwordx2 v61, v[228:229], s[28:29]
	v_pk_mul_f32 v[230:231], v[68:69], v[68:69]
	v_pk_mul_f32 v[232:233], v[70:71], v[70:71]
	v_add_f32_e32 v230, v230, v231
	v_add_f32_e32 v230, v232, v230
	v_add_f32_e32 v236, v233, v230
	v_pk_add_f32 v[84:85], v[84:85], v[36:37]
	v_pk_add_f32 v[86:87], v[86:87], v[38:39]
	global_store_dwordx4 v57, v[84:87], s[10:11] offset:64
	v_pk_mul_f32 v[224:225], v[204:205], v[84:85]
	v_pk_mul_f32 v[226:227], v[206:207], v[86:87]
	v_cvt_pk_bf16_f32 v228, v224, v225
	v_cvt_pk_bf16_f32 v229, v226, v227
	global_store_dwordx2 v61, v[228:229], s[28:29] offset:32
	v_pk_mul_f32 v[230:231], v[84:85], v[84:85]
	v_pk_mul_f32 v[232:233], v[86:87], v[86:87]
	v_add_f32_e32 v230, v230, v231
	v_add_f32_e32 v230, v232, v230
	v_add_f32_e32 v230, v233, v230
	v_add_f32_e32 v236, v236, v230
	v_pk_add_f32 v[100:101], v[100:101], v[52:53]
	v_pk_add_f32 v[102:103], v[102:103], v[54:55]
	global_store_dwordx4 v57, v[100:103], s[10:11] offset:128
	v_pk_mul_f32 v[224:225], v[208:209], v[100:101]
	v_pk_mul_f32 v[226:227], v[210:211], v[102:103]
	v_cvt_pk_bf16_f32 v228, v224, v225
	v_cvt_pk_bf16_f32 v229, v226, v227
	global_store_dwordx2 v61, v[228:229], s[28:29] offset:64
	v_pk_mul_f32 v[230:231], v[100:101], v[100:101]
	v_pk_mul_f32 v[232:233], v[102:103], v[102:103]
	v_add_f32_e32 v230, v230, v231
	v_add_f32_e32 v230, v232, v230
	v_add_f32_e32 v230, v233, v230
	v_add_f32_e32 v236, v236, v230
	v_pk_add_f32 v[116:117], v[116:117], v[252:253]
	v_pk_add_f32 v[118:119], v[118:119], v[254:255]
	global_store_dwordx4 v57, v[116:119], s[10:11] offset:192
	v_pk_mul_f32 v[224:225], v[212:213], v[116:117]
	v_pk_mul_f32 v[226:227], v[214:215], v[118:119]
	v_cvt_pk_bf16_f32 v228, v224, v225
	v_cvt_pk_bf16_f32 v229, v226, v227
	global_store_dwordx2 v61, v[228:229], s[28:29] offset:96
	v_pk_mul_f32 v[230:231], v[116:117], v[116:117]
	v_pk_mul_f32 v[232:233], v[118:119], v[118:119]
	v_add_f32_e32 v230, v230, v231
	v_add_f32_e32 v230, v232, v230
	v_add_f32_e32 v237, v233, v230
	v_pk_add_f32 v[132:133], v[132:133], v[172:173]
	v_pk_add_f32 v[134:135], v[134:135], v[174:175]
	global_store_dwordx4 v57, v[132:135], s[10:11] offset:256
	v_pk_mul_f32 v[224:225], v[216:217], v[132:133]
	v_pk_mul_f32 v[226:227], v[218:219], v[134:135]
	v_cvt_pk_bf16_f32 v228, v224, v225
	v_cvt_pk_bf16_f32 v229, v226, v227
	global_store_dwordx2 v61, v[228:229], s[28:29] offset:128
	v_pk_mul_f32 v[230:231], v[132:133], v[132:133]
	v_pk_mul_f32 v[232:233], v[134:135], v[134:135]
	v_add_f32_e32 v230, v230, v231
	v_add_f32_e32 v230, v232, v230
	v_add_f32_e32 v230, v233, v230
	v_add_f32_e32 v237, v237, v230
	v_pk_add_f32 v[148:149], v[148:149], v[188:189]
	v_pk_add_f32 v[150:151], v[150:151], v[190:191]
	global_store_dwordx4 v57, v[148:151], s[10:11] offset:320
	v_pk_mul_f32 v[224:225], v[220:221], v[148:149]
	v_pk_mul_f32 v[226:227], v[222:223], v[150:151]
	v_cvt_pk_bf16_f32 v228, v224, v225
	v_cvt_pk_bf16_f32 v229, v226, v227
	global_store_dwordx2 v61, v[228:229], s[28:29] offset:160
	v_pk_mul_f32 v[230:231], v[148:149], v[148:149]
	v_pk_mul_f32 v[232:233], v[150:151], v[150:151]
	v_add_f32_e32 v230, v230, v231
	v_add_f32_e32 v230, v232, v230
	v_add_f32_e32 v230, v233, v230
	v_add_f32_e32 v237, v237, v230
	v_pk_add_f32 v[72:73], v[72:73], v[24:25]
	v_pk_add_f32 v[74:75], v[74:75], v[26:27]
	global_store_dwordx4 v58, v[72:75], s[10:11]
	v_pk_mul_f32 v[224:225], v[200:201], v[72:73]
	v_pk_mul_f32 v[226:227], v[202:203], v[74:75]
	v_cvt_pk_bf16_f32 v228, v224, v225
	v_cvt_pk_bf16_f32 v229, v226, v227
	global_store_dwordx2 v62, v[228:229], s[28:29]
	v_pk_mul_f32 v[230:231], v[72:73], v[72:73]
	v_pk_mul_f32 v[232:233], v[74:75], v[74:75]
	v_add_f32_e32 v230, v230, v231
	v_add_f32_e32 v230, v232, v230
	v_add_f32_e32 v238, v233, v230
	v_pk_add_f32 v[88:89], v[88:89], v[40:41]
	v_pk_add_f32 v[90:91], v[90:91], v[42:43]
	global_store_dwordx4 v58, v[88:91], s[10:11] offset:64
	v_pk_mul_f32 v[224:225], v[204:205], v[88:89]
	v_pk_mul_f32 v[226:227], v[206:207], v[90:91]
	v_cvt_pk_bf16_f32 v228, v224, v225
	v_cvt_pk_bf16_f32 v229, v226, v227
	global_store_dwordx2 v62, v[228:229], s[28:29] offset:32
	v_pk_mul_f32 v[230:231], v[88:89], v[88:89]
	v_pk_mul_f32 v[232:233], v[90:91], v[90:91]
	v_add_f32_e32 v230, v230, v231
	v_add_f32_e32 v230, v232, v230
	v_add_f32_e32 v230, v233, v230
	v_add_f32_e32 v238, v238, v230
	v_pk_add_f32 v[104:105], v[104:105], v[240:241]
	v_pk_add_f32 v[106:107], v[106:107], v[242:243]
	global_store_dwordx4 v58, v[104:107], s[10:11] offset:128
	v_pk_mul_f32 v[224:225], v[208:209], v[104:105]
	v_pk_mul_f32 v[226:227], v[210:211], v[106:107]
	v_cvt_pk_bf16_f32 v228, v224, v225
	v_cvt_pk_bf16_f32 v229, v226, v227
	global_store_dwordx2 v62, v[228:229], s[28:29] offset:64
	v_pk_mul_f32 v[230:231], v[104:105], v[104:105]
	v_pk_mul_f32 v[232:233], v[106:107], v[106:107]
	v_add_f32_e32 v230, v230, v231
	v_add_f32_e32 v230, v232, v230
	v_add_f32_e32 v230, v233, v230
	v_add_f32_e32 v238, v238, v230
	v_pk_add_f32 v[120:121], v[120:121], v[160:161]
	v_pk_add_f32 v[122:123], v[122:123], v[162:163]
	global_store_dwordx4 v58, v[120:123], s[10:11] offset:192
	v_pk_mul_f32 v[224:225], v[212:213], v[120:121]
	v_pk_mul_f32 v[226:227], v[214:215], v[122:123]
	v_cvt_pk_bf16_f32 v228, v224, v225
	v_cvt_pk_bf16_f32 v229, v226, v227
	global_store_dwordx2 v62, v[228:229], s[28:29] offset:96
	v_pk_mul_f32 v[230:231], v[120:121], v[120:121]
	v_pk_mul_f32 v[232:233], v[122:123], v[122:123]
	v_add_f32_e32 v230, v230, v231
	v_add_f32_e32 v230, v232, v230
	v_add_f32_e32 v239, v233, v230
	v_pk_add_f32 v[136:137], v[136:137], v[176:177]
	v_pk_add_f32 v[138:139], v[138:139], v[178:179]
	global_store_dwordx4 v58, v[136:139], s[10:11] offset:256
	v_pk_mul_f32 v[224:225], v[216:217], v[136:137]
	v_pk_mul_f32 v[226:227], v[218:219], v[138:139]
	v_cvt_pk_bf16_f32 v228, v224, v225
	v_cvt_pk_bf16_f32 v229, v226, v227
	global_store_dwordx2 v62, v[228:229], s[28:29] offset:128
	v_pk_mul_f32 v[230:231], v[136:137], v[136:137]
	v_pk_mul_f32 v[232:233], v[138:139], v[138:139]
	v_add_f32_e32 v230, v230, v231
	v_add_f32_e32 v230, v232, v230
	v_add_f32_e32 v230, v233, v230
	v_add_f32_e32 v239, v239, v230
	v_pk_add_f32 v[152:153], v[152:153], v[192:193]
	v_pk_add_f32 v[154:155], v[154:155], v[194:195]
	global_store_dwordx4 v58, v[152:155], s[10:11] offset:320
	v_pk_mul_f32 v[224:225], v[220:221], v[152:153]
	v_pk_mul_f32 v[226:227], v[222:223], v[154:155]
	v_cvt_pk_bf16_f32 v228, v224, v225
	v_cvt_pk_bf16_f32 v229, v226, v227
	global_store_dwordx2 v62, v[228:229], s[28:29] offset:160
	v_pk_mul_f32 v[230:231], v[152:153], v[152:153]
	v_pk_mul_f32 v[232:233], v[154:155], v[154:155]
	v_add_f32_e32 v230, v230, v231
	v_add_f32_e32 v230, v232, v230
	v_add_f32_e32 v230, v233, v230
	v_add_f32_e32 v239, v239, v230
	v_pk_add_f32 v[76:77], v[76:77], v[28:29]
	v_pk_add_f32 v[78:79], v[78:79], v[30:31]
	global_store_dwordx4 v59, v[76:79], s[10:11]
	v_pk_mul_f32 v[224:225], v[200:201], v[76:77]
	v_pk_mul_f32 v[226:227], v[202:203], v[78:79]
	v_cvt_pk_bf16_f32 v228, v224, v225
	v_cvt_pk_bf16_f32 v229, v226, v227
	global_store_dwordx2 v63, v[228:229], s[28:29]
	v_pk_mul_f32 v[230:231], v[76:77], v[76:77]
	v_pk_mul_f32 v[232:233], v[78:79], v[78:79]
	v_add_f32_e32 v230, v230, v231
	v_add_f32_e32 v230, v232, v230
	v_add_f32_e32 v14, v233, v230
	v_pk_add_f32 v[92:93], v[92:93], v[44:45]
	v_pk_add_f32 v[94:95], v[94:95], v[46:47]
	global_store_dwordx4 v59, v[92:95], s[10:11] offset:64
	v_pk_mul_f32 v[224:225], v[204:205], v[92:93]
	v_pk_mul_f32 v[226:227], v[206:207], v[94:95]
	v_cvt_pk_bf16_f32 v228, v224, v225
	v_cvt_pk_bf16_f32 v229, v226, v227
	global_store_dwordx2 v63, v[228:229], s[28:29] offset:32
	v_pk_mul_f32 v[230:231], v[92:93], v[92:93]
	v_pk_mul_f32 v[232:233], v[94:95], v[94:95]
	v_add_f32_e32 v230, v230, v231
	v_add_f32_e32 v230, v232, v230
	v_add_f32_e32 v230, v233, v230
	v_add_f32_e32 v14, v14, v230
	v_pk_add_f32 v[108:109], v[108:109], v[244:245]
	v_pk_add_f32 v[110:111], v[110:111], v[246:247]
	global_store_dwordx4 v59, v[108:111], s[10:11] offset:128
	v_pk_mul_f32 v[224:225], v[208:209], v[108:109]
	v_pk_mul_f32 v[226:227], v[210:211], v[110:111]
	v_cvt_pk_bf16_f32 v228, v224, v225
	v_cvt_pk_bf16_f32 v229, v226, v227
	global_store_dwordx2 v63, v[228:229], s[28:29] offset:64
	v_pk_mul_f32 v[230:231], v[108:109], v[108:109]
	v_pk_mul_f32 v[232:233], v[110:111], v[110:111]
	v_add_f32_e32 v230, v230, v231
	v_add_f32_e32 v230, v232, v230
	v_add_f32_e32 v230, v233, v230
	v_add_f32_e32 v14, v14, v230
	v_pk_add_f32 v[124:125], v[124:125], v[164:165]
	v_pk_add_f32 v[126:127], v[126:127], v[166:167]
	global_store_dwordx4 v59, v[124:127], s[10:11] offset:192
	v_pk_mul_f32 v[224:225], v[212:213], v[124:125]
	v_pk_mul_f32 v[226:227], v[214:215], v[126:127]
	v_cvt_pk_bf16_f32 v228, v224, v225
	v_cvt_pk_bf16_f32 v229, v226, v227
	global_store_dwordx2 v63, v[228:229], s[28:29] offset:96
	v_pk_mul_f32 v[230:231], v[124:125], v[124:125]
	v_pk_mul_f32 v[232:233], v[126:127], v[126:127]
	v_add_f32_e32 v230, v230, v231
	v_add_f32_e32 v230, v232, v230
	v_add_f32_e32 v15, v233, v230
	v_pk_add_f32 v[140:141], v[140:141], v[180:181]
	v_pk_add_f32 v[142:143], v[142:143], v[182:183]
	global_store_dwordx4 v59, v[140:143], s[10:11] offset:256
	v_pk_mul_f32 v[224:225], v[216:217], v[140:141]
	v_pk_mul_f32 v[226:227], v[218:219], v[142:143]
	v_cvt_pk_bf16_f32 v228, v224, v225
	v_cvt_pk_bf16_f32 v229, v226, v227
	global_store_dwordx2 v63, v[228:229], s[28:29] offset:128
	v_pk_mul_f32 v[230:231], v[140:141], v[140:141]
	v_pk_mul_f32 v[232:233], v[142:143], v[142:143]
	v_add_f32_e32 v230, v230, v231
	v_add_f32_e32 v230, v232, v230
	v_add_f32_e32 v230, v233, v230
	v_add_f32_e32 v15, v15, v230
	v_pk_add_f32 v[156:157], v[156:157], v[196:197]
	v_pk_add_f32 v[158:159], v[158:159], v[198:199]
	global_store_dwordx4 v59, v[156:159], s[10:11] offset:320
	v_pk_mul_f32 v[224:225], v[220:221], v[156:157]
	v_pk_mul_f32 v[226:227], v[222:223], v[158:159]
	v_cvt_pk_bf16_f32 v228, v224, v225
	v_cvt_pk_bf16_f32 v229, v226, v227
	global_store_dwordx2 v63, v[228:229], s[28:29] offset:160
	v_pk_mul_f32 v[230:231], v[156:157], v[156:157]
	v_pk_mul_f32 v[232:233], v[158:159], v[158:159]
	v_add_f32_e32 v230, v230, v231
	v_add_f32_e32 v230, v232, v230
	v_add_f32_e32 v230, v233, v230
	v_add_f32_e32 v15, v15, v230
	ds_bpermute_b32 v224, v13, v234
	ds_bpermute_b32 v225, v13, v235
	ds_bpermute_b32 v226, v13, v236
	ds_bpermute_b32 v227, v13, v237
	ds_bpermute_b32 v228, v13, v238
	ds_bpermute_b32 v229, v13, v239
	ds_bpermute_b32 v230, v13, v14
	ds_bpermute_b32 v231, v13, v15
	s_waitcnt lgkmcnt(0)
	v_add_f32_e32 v234, v234, v224
	v_add_f32_e32 v235, v235, v225
	v_add_f32_e32 v236, v236, v226
	v_add_f32_e32 v237, v237, v227
	v_add_f32_e32 v238, v238, v228
	v_add_f32_e32 v239, v239, v229
	v_add_f32_e32 v14, v14, v230
	v_add_f32_e32 v15, v15, v231
	ds_bpermute_b32 v224, v12, v234
	ds_bpermute_b32 v225, v12, v235
	ds_bpermute_b32 v226, v12, v236
	ds_bpermute_b32 v227, v12, v237
	ds_bpermute_b32 v228, v12, v238
	ds_bpermute_b32 v229, v12, v239
	ds_bpermute_b32 v230, v12, v14
	ds_bpermute_b32 v231, v12, v15
	s_waitcnt lgkmcnt(0)
	v_add_f32_e32 v234, v234, v224
	v_add_f32_e32 v235, v235, v225
	v_add_f32_e32 v236, v236, v226
	v_add_f32_e32 v237, v237, v227
	v_add_f32_e32 v238, v238, v228
	v_add_f32_e32 v239, v239, v229
	v_add_f32_e32 v14, v14, v230
	v_add_f32_e32 v15, v15, v231
	s_and_saveexec_b64 s[2:3], vcc
	global_store_dwordx2 v8, v[234:235], s[26:27]
	global_store_dwordx2 v9, v[236:237], s[26:27]
	global_store_dwordx2 v10, v[238:239], s[26:27]
	global_store_dwordx2 v11, v[14:15], s[26:27]
	s_or_b64 exec, exec, s[2:3]
